# baseline (speedup 1.0000x reference)
.LBB1_1:
	v_mfma_f32_32x32x64_f8f6f4 v[76:91], v[84:91], v[116:123], v[36:51]
	v_cvt_pk_fp8_f32 v132, v161, v163
	v_add_u32_e32 v68, s36, v176
	v_cvt_pk_fp8_f32 v132, v162, v164 op_sel:[0,0,1]
	ds_read_b128 v[162:165], v68 offset:49152
	ds_read_b128 v[166:169], v68 offset:50176
	v_cvt_pk_fp8_f32 v133, v150, v154
	v_cvt_pk_fp8_f32 v133, v152, v157 op_sel:[0,0,1]
	s_lshl_b32 s16, s12, 12
	s_add_i32 s15, s16, 0x3000
	s_add_i32 s17, s14, s33
	s_mov_b32 m0, s17
	s_nop 0
	buffer_load_dwordx4 v174, s[20:23], s15 offen lds
	v_cvt_pk_fp8_f32 v134, v149, v153
	v_cvt_pk_fp8_f32 v134, v151, v156 op_sel:[0,0,1]
	v_cvt_pk_fp8_f32 v135, v155, v159
	v_cvt_pk_fp8_f32 v135, v158, v160 op_sel:[0,0,1]
	v_cvt_pk_fp8_f32 v136, v100, v148
	v_cvt_pk_fp8_f32 v136, v101, v102 op_sel:[0,0,1]
	s_waitcnt lgkmcnt(2)
	v_mfma_f32_32x32x64_f8f6f4 v[92:107], v[92:99], v[116:123], v[36:51]
	ds_read_b128 v[148:151], v68 offset:49664
	ds_read_b128 v[152:155], v68 offset:50688
	v_cvt_pk_fp8_f32 v137, v143, v146
	v_cvt_pk_fp8_f32 v137, v145, v147 op_sel:[0,0,1]
	s_add_i32 s15, s16, 0x1000
	s_add_i32 s17, s13, s34
	s_mov_b32 m0, s17
	s_nop 0
	buffer_load_dwordx4 v174, s[24:27], s15 offen lds
	v_cvt_pk_fp8_f32 v138, v69, v109
	v_cvt_pk_fp8_f32 v138, v108, v142 op_sel:[0,0,1]
	v_cvt_pk_fp8_f32 v139, v110, v144
	v_cvt_pk_fp8_f32 v139, v111, v114 op_sel:[0,0,1]
	s_waitcnt lgkmcnt(2)
	s_nop 0
	v_mfma_f32_32x32x64_f8f6f4 v[4:19], v[162:169], v[132:139], v[4:19]
	v_exp_f32_e32 v142, v76
	v_exp_f32_e32 v143, v77
	v_exp_f32_e32 v144, v78
	v_exp_f32_e32 v145, v79
	v_exp_f32_e32 v146, v80
	v_exp_f32_e32 v147, v81
	v_exp_f32_e32 v156, v82
	v_exp_f32_e32 v157, v83
	v_add_u32_e32 v158, s13, v176
	ds_read_b128 v[108:111], v158
	ds_read_b128 v[112:115], v158 offset:1024
	ds_read_b128 v[52:55], v158 offset:512
	ds_read_b128 v[56:59], v158 offset:1536
	v_exp_f32_e32 v159, v84
	v_exp_f32_e32 v160, v85
	v_mfma_f32_16x16x128_f8f6f4 v[200:203], v[124:131], v[132:139], v[200:203]
	v_exp_f32_e32 v161, v86
	v_exp_f32_e32 v162, v87
	v_exp_f32_e32 v163, v88
	v_exp_f32_e32 v164, v89
	v_exp_f32_e32 v165, v90
	v_exp_f32_e32 v166, v91
	s_waitcnt lgkmcnt(4)
	v_mfma_f32_32x32x64_f8f6f4 v[20:35], v[148:155], v[132:139], v[20:35]
	v_exp_f32_e32 v167, v92
	v_exp_f32_e32 v168, v93
	v_exp_f32_e32 v169, v94
	v_exp_f32_e32 v170, v95
	v_exp_f32_e32 v148, v96
	v_exp_f32_e32 v149, v97
	v_exp_f32_e32 v150, v98
	v_exp_f32_e32 v151, v99
	v_exp_f32_e32 v152, v100
	v_exp_f32_e32 v153, v101
	v_exp_f32_e32 v154, v102
	v_exp_f32_e32 v155, v103
	v_exp_f32_e32 v158, v104
	v_exp_f32_e32 v171, v105
	v_exp_f32_e32 v177, v106
	v_exp_f32_e32 v186, v107
	s_add_i32 s15, s13, 0x4000
	s_cmpk_lg_u32 s13, 0x8000
	s_cselect_b32 s15, s15, 0
	s_waitcnt vmcnt(2) lgkmcnt(0)
	s_barrier
	v_mfma_f32_32x32x64_f8f6f4 v[84:99], v[108:115], v[116:123], v[36:51]
	v_cvt_pk_fp8_f32 v132, v142, v143
	v_add_u32_e32 v142, s14, v176
	v_cvt_pk_fp8_f32 v132, v144, v145 op_sel:[0,0,1]
	ds_read_b128 v[60:63], v142 offset:49152
	ds_read_b128 v[64:67], v142 offset:50176
	v_cvt_pk_fp8_f32 v133, v146, v147
	v_cvt_pk_fp8_f32 v133, v156, v157 op_sel:[0,0,1]
	s_add_i32 s14, s16, 0x4000
	s_add_i32 s17, s13, s33
	s_mov_b32 m0, s17
	s_nop 0
	buffer_load_dwordx4 v174, s[20:23], s14 offen lds
	v_cvt_pk_fp8_f32 v134, v159, v160
	v_cvt_pk_fp8_f32 v134, v161, v162 op_sel:[0,0,1]
	v_cvt_pk_fp8_f32 v135, v163, v164
	v_cvt_pk_fp8_f32 v135, v165, v166 op_sel:[0,0,1]
	s_waitcnt lgkmcnt(2)
	v_mfma_f32_32x32x64_f8f6f4 v[100:115], v[52:59], v[116:123], v[36:51]
	v_cvt_pk_fp8_f32 v136, v167, v168
	v_cvt_pk_fp8_f32 v136, v169, v170 op_sel:[0,0,1]
	ds_read_b128 v[178:181], v142 offset:49664
	ds_read_b128 v[182:185], v142 offset:50688
	v_cvt_pk_fp8_f32 v137, v148, v149
	v_cvt_pk_fp8_f32 v137, v150, v151 op_sel:[0,0,1]
	s_addk_i32 s16, 0x2000
	s_add_i32 s14, s15, s34
	s_mov_b32 m0, s14
	s_nop 0
	buffer_load_dwordx4 v174, s[24:27], s16 offen lds
	v_cvt_pk_fp8_f32 v138, v152, v153
	v_cvt_pk_fp8_f32 v138, v154, v155 op_sel:[0,0,1]
	v_cvt_pk_fp8_f32 v139, v158, v171
	v_cvt_pk_fp8_f32 v139, v177, v186 op_sel:[0,0,1]
	v_sub_f32_e32 v52, v200, v204
	v_mov_b32_e32 v204, v200
	v_max_f32_e32 v0, v0, v0
	v_max_f32_e32 v0, v0, v52
	s_waitcnt lgkmcnt(2)
	v_mfma_f32_32x32x64_f8f6f4 v[4:19], v[60:67], v[132:139], v[4:19]
	v_exp_f32_e32 v161, v84
	v_exp_f32_e32 v163, v85
	v_exp_f32_e32 v162, v86
	v_exp_f32_e32 v164, v87
	v_exp_f32_e32 v150, v88
	v_exp_f32_e32 v154, v89
	v_exp_f32_e32 v152, v90
	v_exp_f32_e32 v157, v91
	v_add_u32_e32 v141, s15, v176
	ds_read_b128 v[84:87], v141
	ds_read_b128 v[88:91], v141 offset:1024
	v_mfma_f32_16x16x128_f8f6f4 v[200:203], v[124:131], v[132:139], v[200:203]
	v_exp_f32_e32 v149, v92
	v_exp_f32_e32 v153, v93
	v_exp_f32_e32 v151, v94
	v_exp_f32_e32 v156, v95
	v_exp_f32_e32 v155, v96
	v_exp_f32_e32 v159, v97
	v_exp_f32_e32 v158, v98
	v_exp_f32_e32 v160, v99
	ds_read_b128 v[92:95], v141 offset:512
	ds_read_b128 v[96:99], v141 offset:1536
	s_waitcnt lgkmcnt(4)
	v_mfma_f32_32x32x64_f8f6f4 v[20:35], v[178:185], v[132:139], v[20:35]
	v_exp_f32_e32 v100, v100
	v_exp_f32_e32 v148, v101
	v_exp_f32_e32 v101, v102
	v_exp_f32_e32 v102, v103
	v_exp_f32_e32 v143, v104
	v_exp_f32_e32 v146, v105
	v_exp_f32_e32 v145, v106
	v_exp_f32_e32 v147, v107
	v_exp_f32_e32 v69, v108
	v_exp_f32_e32 v109, v109
	v_exp_f32_e32 v108, v110
	v_exp_f32_e32 v142, v111
	v_exp_f32_e32 v110, v112
	v_exp_f32_e32 v144, v113
	v_exp_f32_e32 v111, v114
	v_exp_f32_e32 v114, v115
	s_add_i32 s16, s15, 0x4000
	s_cmpk_lg_u32 s15, 0x8000
	s_mov_b32 s36, s13
	s_mov_b32 s14, s15
	s_cselect_b32 s13, s16, 0
	s_add_i32 s12, s12, 2
	s_cmp_gt_u32 s12, 26
	s_waitcnt vmcnt(2) lgkmcnt(0)
	s_barrier
	s_cbranch_scc0 .LBB1_1
	s_and_b32 s41, s2, 3
	s_lshl_b32 s42, s41, 6
	s_lshl_b32 s43, s3, 5
	s_add_i32 s42, s42, s43
	v_add_u32_e32 v198, s42, v172
	v_lshlrev_b32_e32 v198, 8, v198
	v_lshl_add_u32 v198, v175, 4, v198
	s_lshl_b32 s44, s41, 8
	s_lshl_b32 s45, s3, 7
	s_add_i32 s44, s44, s45
	v_lshl_add_u32 v199, v175, 4, s44
	s_lshl_b32 s46, s41, 2
	v_mov_b32_e32 v205, s46
	v_add_u32_e32 v113, 0xc000, v176
	v_mov_b32_e32 v112, 0x7f7f7f7f
	v_cvt_pk_fp8_f32 v132, v161, v163
	v_cvt_pk_fp8_f32 v132, v162, v164 op_sel:[0,0,1]
	s_waitcnt lgkmcnt(2)
	v_mfma_f32_32x32x64_f8f6f4 v[70:85], v[84:91], v[116:123], v[36:51]
	ds_read_b128 v[162:165], v113 offset:32768
	ds_read_b128 v[166:169], v113 offset:33792
	v_cvt_pk_fp8_f32 v133, v150, v154
	v_cvt_pk_fp8_f32 v133, v152, v157 op_sel:[0,0,1]
	s_mov_b32 s13, 0x1e000
	s_mov_b32 m0, s33
	s_nop 0
	buffer_load_dwordx4 v174, s[20:23], s13 offen lds
	v_cvt_pk_fp8_f32 v134, v149, v153
	v_cvt_pk_fp8_f32 v134, v151, v156 op_sel:[0,0,1]
	v_cvt_pk_fp8_f32 v135, v155, v159
	v_cvt_pk_fp8_f32 v135, v158, v160 op_sel:[0,0,1]
	v_cvt_pk_fp8_f32 v136, v100, v148
	v_cvt_pk_fp8_f32 v136, v101, v102 op_sel:[0,0,1]
	s_waitcnt lgkmcnt(2)
	v_mfma_f32_32x32x64_f8f6f4 v[86:101], v[92:99], v[116:123], v[36:51]
	ds_read_b128 v[148:151], v113 offset:33280
	ds_read_b128 v[152:155], v113 offset:34304
	v_cvt_pk_fp8_f32 v137, v143, v146
	v_cvt_pk_fp8_f32 v137, v145, v147 op_sel:[0,0,1]
	s_cmp_lg_u32 0, -1
	s_cselect_b32 s12, 0, 0
	s_add_i32 s15, s12, s35
	s_add_i32 s12, s15, 0x10000
	s_mov_b32 s26, s22
	s_mov_b32 s27, s23
	s_mov_b32 s14, 0x1c000
	s_mov_b32 m0, s12
	s_nop 0
	buffer_load_dwordx4 v174, s[24:27], s14 offen lds
	global_load_dwordx4 v[208:211], v198, s[4:5]
	global_load_dwordx4 v[212:215], v198, s[4:5] offset:32
	global_load_dwordx4 v[216:219], v198, s[4:5] offset:64
	global_load_dwordx4 v[220:223], v198, s[4:5] offset:96
	global_load_dwordx4 v[224:227], v198, s[4:5] offset:128
	v_cvt_pk_fp8_f32 v138, v69, v109
	v_cvt_pk_fp8_f32 v138, v108, v142 op_sel:[0,0,1]
	v_cvt_pk_fp8_f32 v139, v110, v144
	v_cvt_pk_fp8_f32 v139, v111, v114 op_sel:[0,0,1]
	s_waitcnt lgkmcnt(2)
	s_nop 0
	v_mfma_f32_32x32x64_f8f6f4 v[4:19], v[162:169], v[132:139], v[4:19]
	v_exp_f32_e32 v104, v73
	v_exp_f32_e32 v69, v70
	v_exp_f32_e32 v102, v71
	v_exp_f32_e32 v103, v72
	v_exp_f32_e32 v110, v74
	v_exp_f32_e32 v111, v75
	v_exp_f32_e32 v114, v76
	v_exp_f32_e32 v115, v77
	ds_read_b128 v[70:73], v176 offset:16384
	ds_read_b128 v[74:77], v176 offset:17408
	v_mfma_f32_16x16x128_f8f6f4 v[200:203], v[124:131], v[132:139], v[200:203]
	v_exp_f32_e32 v140, v78
	v_exp_f32_e32 v141, v79
	v_exp_f32_e32 v142, v80
	v_exp_f32_e32 v143, v81
	v_exp_f32_e32 v144, v82
	v_exp_f32_e32 v145, v83
	v_exp_f32_e32 v146, v84
	v_exp_f32_e32 v147, v85
	s_waitcnt lgkmcnt(2)
	v_mfma_f32_32x32x64_f8f6f4 v[20:35], v[148:155], v[132:139], v[20:35]
	v_exp_f32_e32 v156, v86
	v_exp_f32_e32 v157, v87
	v_exp_f32_e32 v158, v88
	v_exp_f32_e32 v159, v89
	v_exp_f32_e32 v148, v90
	v_exp_f32_e32 v149, v91
	v_exp_f32_e32 v150, v92
	v_exp_f32_e32 v151, v93
	ds_read_b128 v[86:89], v176 offset:16896
	ds_read_b128 v[90:93], v176 offset:17920
	v_exp_f32_e32 v152, v94
	v_exp_f32_e32 v153, v95
	v_exp_f32_e32 v154, v96
	v_exp_f32_e32 v155, v97
	v_exp_f32_e32 v160, v98
	v_exp_f32_e32 v161, v99
	v_exp_f32_e32 v162, v100
	v_exp_f32_e32 v163, v101
	s_waitcnt vmcnt(7) lgkmcnt(0)
	s_barrier
	s_waitcnt lgkmcnt(2)
	v_mfma_f32_32x32x64_f8f6f4 v[70:85], v[70:77], v[116:123], v[36:51]
	v_cvt_pk_fp8_f32 v132, v69, v102
	v_cvt_pk_fp8_f32 v132, v103, v104 op_sel:[0,0,1]
	ds_read_b128 v[102:105], v176 offset:49152
	ds_read_b128 v[106:109], v176 offset:50176
	v_cvt_pk_fp8_f32 v133, v110, v111
	v_cvt_pk_fp8_f32 v133, v114, v115 op_sel:[0,0,1]
	s_add_i32 s16, s15, 0x4000
	s_mov_b32 s14, 0x1f000
	s_mov_b32 m0, s16
	s_nop 0
	buffer_load_dwordx4 v174, s[20:23], s14 offen lds
	v_cvt_pk_fp8_f32 v134, v140, v141
	v_cvt_pk_fp8_f32 v134, v142, v143 op_sel:[0,0,1]
	v_cvt_pk_fp8_f32 v135, v144, v145
	v_cvt_pk_fp8_f32 v135, v146, v147 op_sel:[0,0,1]
	s_waitcnt lgkmcnt(2)
	v_mfma_f32_32x32x64_f8f6f4 v[86:101], v[86:93], v[116:123], v[36:51]
	v_cvt_pk_fp8_f32 v136, v156, v157
	v_cvt_pk_fp8_f32 v136, v158, v159 op_sel:[0,0,1]
	ds_read_b128 v[140:143], v176 offset:49664
	ds_read_b128 v[144:147], v176 offset:50688
	v_cvt_pk_fp8_f32 v137, v148, v149
	v_cvt_pk_fp8_f32 v137, v150, v151 op_sel:[0,0,1]
	s_add_i32 s15, s15, 0x14000
	s_mov_b32 s16, 0x1d000
	s_mov_b32 m0, s15
	s_nop 0
	buffer_load_dwordx4 v174, s[24:27], s16 offen lds
	global_load_dwordx4 v[228:231], v198, s[4:5] offset:160
	global_load_dwordx4 v[232:235], v198, s[4:5] offset:192
	global_load_dwordx4 v[236:239], v198, s[4:5] offset:224
	global_load_dwordx4 v[240:243], v199, s[6:7]
	v_cvt_pk_fp8_f32 v138, v152, v153
	v_cvt_pk_fp8_f32 v138, v154, v155 op_sel:[0,0,1]
	v_cvt_pk_fp8_f32 v139, v160, v161
	v_cvt_pk_fp8_f32 v139, v162, v163 op_sel:[0,0,1]
	v_sub_f32_e32 v114, v200, v204
	v_mov_b32_e32 v204, v200
	s_waitcnt lgkmcnt(2)
	v_mfma_f32_32x32x64_f8f6f4 v[4:19], v[102:109], v[132:139], v[4:19]
	v_exp_f32_e32 v110, v70
	v_exp_f32_e32 v111, v71
	v_exp_f32_e32 v148, v73
	v_exp_f32_e32 v115, v72
	v_exp_f32_e32 v149, v74
	v_exp_f32_e32 v150, v75
	v_exp_f32_e32 v151, v76
	v_exp_f32_e32 v152, v77
	ds_read_b128 v[70:73], v176 offset:32768
	ds_read_b128 v[74:77], v176 offset:33792
	v_mfma_f32_16x16x128_f8f6f4 v[200:203], v[124:131], v[132:139], v[200:203]
	v_exp_f32_e32 v153, v78
	v_exp_f32_e32 v154, v79
	v_exp_f32_e32 v155, v80
	v_exp_f32_e32 v156, v81
	v_exp_f32_e32 v157, v83
	v_exp_f32_e32 v158, v84
	v_exp_f32_e32 v159, v85
	s_nop 7
	v_exp_f32_e32 v53, v82
	s_waitcnt lgkmcnt(2)
	v_mfma_f32_32x32x64_f8f6f4 v[20:35], v[140:147], v[132:139], v[20:35]
	v_exp_f32_e32 v160, v86
	v_exp_f32_e32 v161, v87
	v_exp_f32_e32 v162, v88
	v_exp_f32_e32 v163, v89
	v_exp_f32_e32 v164, v90
	v_exp_f32_e32 v165, v91
	v_exp_f32_e32 v166, v92
	v_exp_f32_e32 v167, v93
	ds_read_b128 v[78:81], v176 offset:33280
	ds_read_b128 v[82:85], v176 offset:34304
	v_exp_f32_e32 v168, v94
	v_exp_f32_e32 v169, v95
	v_exp_f32_e32 v170, v96
	v_exp_f32_e32 v171, v97
	v_exp_f32_e32 v177, v98
	v_exp_f32_e32 v178, v99
	v_exp_f32_e32 v179, v100
	v_exp_f32_e32 v180, v101
	s_waitcnt vmcnt(11) lgkmcnt(0)
	s_barrier
	s_waitcnt lgkmcnt(2)
	v_mfma_f32_32x32x64_f8f6f4 v[86:101], v[70:77], v[116:123], v[36:51]
	v_cvt_pk_fp8_f32 v132, v110, v111
	v_cvt_pk_fp8_f32 v132, v115, v148 op_sel:[0,0,1]
	ds_read_b128 v[102:105], v113 offset:16384
	ds_read_b128 v[106:109], v113 offset:17408
	v_cvt_pk_fp8_f32 v133, v149, v150
	v_cvt_pk_fp8_f32 v133, v151, v152 op_sel:[0,0,1]
	v_cvt_pk_fp8_f32 v134, v153, v154
	v_cvt_pk_fp8_f32 v134, v155, v156 op_sel:[0,0,1]
	v_cvt_pk_fp8_f32 v135, v53, v157
	v_cvt_pk_fp8_f32 v135, v158, v159 op_sel:[0,0,1]
	s_waitcnt lgkmcnt(2)
	v_mfma_f32_32x32x64_f8f6f4 v[70:85], v[78:85], v[116:123], v[36:51]
	v_cvt_pk_fp8_f32 v136, v160, v161
	v_cvt_pk_fp8_f32 v136, v162, v163 op_sel:[0,0,1]
	ds_read_b128 v[140:143], v113 offset:16896
	ds_read_b128 v[144:147], v113 offset:17920
	v_cvt_pk_fp8_f32 v137, v164, v165
	v_cvt_pk_fp8_f32 v137, v166, v167 op_sel:[0,0,1]
	s_mov_b32 m0, s34
	s_nop 0
	buffer_load_dwordx4 v174, s[24:27], s13 offen lds
	global_load_dwordx4 v[244:247], v199, s[6:7] offset:32
	global_load_dwordx4 v[248:251], v199, s[6:7] offset:64
	global_load_dwordx4 v[252:255], v199, s[6:7] offset:96
	global_load_dword v205, v205, s[8:9]
	v_cvt_pk_fp8_f32 v138, v168, v169
	v_cvt_pk_fp8_f32 v138, v170, v171 op_sel:[0,0,1]
	v_cvt_pk_fp8_f32 v139, v177, v178
	v_cvt_pk_fp8_f32 v139, v179, v180 op_sel:[0,0,1]
	s_waitcnt lgkmcnt(2)
	s_nop 0
	v_mfma_f32_32x32x64_f8f6f4 v[4:19], v[102:109], v[132:139], v[4:19]
	v_exp_f32_e32 v148, v88
	v_exp_f32_e32 v149, v89
	v_exp_f32_e32 v53, v86
	v_exp_f32_e32 v115, v87
	v_exp_f32_e32 v150, v92
	v_exp_f32_e32 v151, v93
	v_exp_f32_e32 v102, v90
	v_exp_f32_e32 v103, v91
	ds_read_b128 v[86:89], v176
	ds_read_b128 v[90:93], v176 offset:1024
	v_mfma_f32_16x16x128_f8f6f4 v[200:203], v[124:131], v[132:139], v[200:203]
	v_exp_f32_e32 v152, v94
	v_exp_f32_e32 v153, v95
	v_exp_f32_e32 v154, v96
	v_exp_f32_e32 v155, v97
	v_exp_f32_e32 v156, v98
	v_exp_f32_e32 v157, v99
	v_exp_f32_e32 v158, v100
	v_exp_f32_e32 v159, v101
	s_waitcnt lgkmcnt(2)
	v_mfma_f32_32x32x64_f8f6f4 v[20:35], v[140:147], v[132:139], v[20:35]
	v_exp_f32_e32 v160, v70
	v_exp_f32_e32 v161, v71
	v_exp_f32_e32 v162, v72
	v_exp_f32_e32 v163, v73
	v_exp_f32_e32 v164, v74
	v_exp_f32_e32 v165, v75
	v_exp_f32_e32 v166, v76
	v_exp_f32_e32 v167, v77
	ds_read_b128 v[94:97], v176 offset:512
	ds_read_b128 v[98:101], v176 offset:1536
	v_exp_f32_e32 v168, v78
	v_exp_f32_e32 v169, v79
	v_exp_f32_e32 v170, v80
	v_exp_f32_e32 v171, v81
	v_exp_f32_e32 v177, v82
	v_exp_f32_e32 v178, v83
	v_exp_f32_e32 v179, v84
	v_exp_f32_e32 v180, v85
	s_waitcnt vmcnt(9) lgkmcnt(0)
	s_barrier
	s_waitcnt lgkmcnt(2)
	v_mfma_f32_32x32x64_f8f6f4 v[70:85], v[86:93], v[116:123], v[36:51]
	ds_read_b128 v[104:107], v113 offset:32768
	ds_read_b128 v[108:111], v113 offset:33792
	v_cvt_pk_fp8_f32 v132, v53, v115
	v_cvt_pk_fp8_f32 v133, v102, v103
	v_cvt_pk_fp8_f32 v134, v152, v153
	v_cvt_pk_fp8_f32 v132, v148, v149 op_sel:[0,0,1]
	v_cvt_pk_fp8_f32 v133, v150, v151 op_sel:[0,0,1]
	v_cvt_pk_fp8_f32 v134, v154, v155 op_sel:[0,0,1]
	v_cvt_pk_fp8_f32 v135, v156, v157
	v_cvt_pk_fp8_f32 v135, v158, v159 op_sel:[0,0,1]
	s_waitcnt lgkmcnt(2)
	v_mfma_f32_32x32x64_f8f6f4 v[86:101], v[94:101], v[116:123], v[36:51]
	v_cvt_pk_fp8_f32 v136, v160, v161
	v_cvt_pk_fp8_f32 v136, v162, v163 op_sel:[0,0,1]
	ds_read_b128 v[140:143], v113 offset:33280
	ds_read_b128 v[144:147], v113 offset:34304
	v_cvt_pk_fp8_f32 v137, v164, v165
	v_cvt_pk_fp8_f32 v137, v166, v167 op_sel:[0,0,1]
	s_mov_b32 m0, s12
	s_nop 0
	buffer_load_dwordx4 v174, s[24:27], s14 offen lds
	v_cvt_pk_fp8_f32 v138, v168, v169
	v_cvt_pk_fp8_f32 v138, v170, v171 op_sel:[0,0,1]
	v_cvt_pk_fp8_f32 v139, v177, v178
	v_cvt_pk_fp8_f32 v139, v179, v180 op_sel:[0,0,1]
	v_sub_f32_e32 v52, v200, v204
	v_mov_b32_e32 v204, v200
	v_max3_f32 v0, v0, v114, v52
	v_exp_f32_e32 v72, v72
	v_exp_f32_e32 v73, v73
	v_exp_f32_e32 v52, v70
	v_exp_f32_e32 v53, v71
	v_exp_f32_e32 v102, v74
	v_exp_f32_e32 v103, v75
	v_exp_f32_e32 v114, v76
	v_exp_f32_e32 v115, v77
	ds_read_b128 v[150:153], v176 offset:16384
	ds_read_b128 v[154:157], v176 offset:17408
	v_mfma_f32_16x16x128_f8f6f4 v[200:203], v[124:131], v[132:139], v[200:203]
	v_exp_f32_e32 v177, v78
	v_exp_f32_e32 v178, v79
	v_exp_f32_e32 v179, v80
	v_exp_f32_e32 v180, v81
	s_nop 10
	v_exp_f32_e32 v55, v82
	v_exp_f32_e32 v181, v83
	v_exp_f32_e32 v182, v84
	v_exp_f32_e32 v183, v85
	v_exp_f32_e32 v184, v86
	v_exp_f32_e32 v185, v87
	v_exp_f32_e32 v88, v88
	v_exp_f32_e32 v89, v89
	v_exp_f32_e32 v186, v90
	v_exp_f32_e32 v187, v91
	v_exp_f32_e32 v188, v92
	v_exp_f32_e32 v189, v93
	ds_read_b128 v[164:167], v176 offset:16896
	ds_read_b128 v[168:171], v176 offset:17920
	v_exp_f32_e32 v190, v94
	v_exp_f32_e32 v191, v95
	v_exp_f32_e32 v192, v96
	v_exp_f32_e32 v193, v97
	v_exp_f32_e32 v194, v98
	v_exp_f32_e32 v195, v99
	v_exp_f32_e32 v196, v100
	v_exp_f32_e32 v197, v101
	s_waitcnt vmcnt(0) lgkmcnt(0)
	s_barrier
	v_mov_b32_e32 v148, v132
	v_cvt_pk_fp8_f32 v148, v52, v53
	v_cvt_pk_fp8_f32 v148, v72, v73 op_sel:[0,0,1]
	s_waitcnt lgkmcnt(2)
	v_mfma_f32_32x32x64_f8f6f4 v[72:87], v[150:157], v[116:123], v[36:51]
	ds_read_b128 v[156:159], v176 offset:49152
	ds_read_b128 v[160:163], v176 offset:50176
	v_mov_b32_e32 v149, v133
	v_cvt_pk_fp8_f32 v149, v102, v103
	v_cvt_pk_fp8_f32 v149, v114, v115 op_sel:[0,0,1]
	v_mov_b32_e32 v150, v134
	v_cvt_pk_fp8_f32 v150, v177, v178
	v_cvt_pk_fp8_f32 v150, v179, v180 op_sel:[0,0,1]
	v_mov_b32_e32 v151, v135
	v_cvt_pk_fp8_f32 v151, v55, v181
	v_cvt_pk_fp8_f32 v151, v182, v183 op_sel:[0,0,1]
	v_mov_b32_e32 v152, v136
	v_cvt_pk_fp8_f32 v152, v184, v185
	v_cvt_pk_fp8_f32 v152, v88, v89 op_sel:[0,0,1]
	s_waitcnt lgkmcnt(2)
	v_mfma_f32_32x32x64_f8f6f4 v[88:103], v[164:171], v[116:123], v[36:51]
	ds_read_b128 v[164:167], v176 offset:49664
	ds_read_b128 v[168:171], v176 offset:50688
	v_mov_b32_e32 v153, v137
	v_cvt_pk_fp8_f32 v153, v186, v187
	v_cvt_pk_fp8_f32 v153, v188, v189 op_sel:[0,0,1]
	v_mov_b32_e32 v154, v138
	v_cvt_pk_fp8_f32 v154, v190, v191
	v_cvt_pk_fp8_f32 v154, v192, v193 op_sel:[0,0,1]
	v_mov_b32_e32 v155, v139
	v_cvt_pk_fp8_f32 v155, v194, v195
	v_cvt_pk_fp8_f32 v155, v196, v197 op_sel:[0,0,1]
	v_sub_f32_e32 v52, v200, v204
	v_mov_b32_e32 v204, v200
	s_nop 2
	v_exp_f32_e32 v36, v72
	v_exp_f32_e32 v37, v73
	v_exp_f32_e32 v38, v74
	v_exp_f32_e32 v39, v75
	v_exp_f32_e32 v40, v76
	v_exp_f32_e32 v41, v77
	v_exp_f32_e32 v42, v78
	v_exp_f32_e32 v43, v79
	v_exp_f32_e32 v53, v80
	v_exp_f32_e32 v80, v83
	v_exp_f32_e32 v54, v81
	v_exp_f32_e32 v55, v82
	v_exp_f32_e32 v81, v84
	v_exp_f32_e32 v82, v85
	v_exp_f32_e32 v83, v86
	v_exp_f32_e32 v84, v87
	v_exp_f32_e32 v44, v88
	v_exp_f32_e32 v45, v89
	v_exp_f32_e32 v46, v90
	v_exp_f32_e32 v47, v91
	v_exp_f32_e32 v48, v92
	v_exp_f32_e32 v49, v93
	v_exp_f32_e32 v50, v94
	v_exp_f32_e32 v51, v95
	v_exp_f32_e32 v75, v96
	v_exp_f32_e32 v85, v97
	v_exp_f32_e32 v86, v98
	v_exp_f32_e32 v87, v99
	v_exp_f32_e32 v88, v100
	v_exp_f32_e32 v89, v101
	v_exp_f32_e32 v90, v102
	v_exp_f32_e32 v91, v103
	v_mov_b32_e32 v72, 0
	v_mov_b32_e32 v76, 0
	v_mov_b32_e32 v73, 0
	v_mov_b32_e32 v77, 0
	v_cvt_pk_fp8_f32 v72, v36, v37
	v_cvt_pk_fp8_f32 v76, v44, v45
	v_cvt_pk_fp8_f32 v73, v40, v41
	v_cvt_pk_fp8_f32 v77, v48, v49
	v_cvt_pk_fp8_f32 v72, v38, v39 op_sel:[0,0,1]
	v_cvt_pk_fp8_f32 v76, v46, v47 op_sel:[0,0,1]
	v_cvt_pk_fp8_f32 v73, v42, v43 op_sel:[0,0,1]
	v_cvt_pk_fp8_f32 v77, v50, v51 op_sel:[0,0,1]
	v_mfma_f32_16x16x128_f8f6f4 v[200:203], v[124:131], v[148:155], v[200:203]
	v_mov_b32_e32 v78, 0
	v_mov_b32_e32 v79, 0
	v_mov_b32_e32 v74, 0
	v_cvt_pk_fp8_f32 v78, v75, v85
	v_mov_b32_e32 v75, 0
	v_cvt_pk_fp8_f32 v74, v53, v54
	v_cvt_pk_fp8_f32 v75, v81, v82
	v_cvt_pk_fp8_f32 v79, v88, v89
	v_cvt_pk_fp8_f32 v78, v86, v87 op_sel:[0,0,1]
	v_cvt_pk_fp8_f32 v74, v55, v80 op_sel:[0,0,1]
	v_cvt_pk_fp8_f32 v75, v83, v84 op_sel:[0,0,1]
	v_cvt_pk_fp8_f32 v79, v90, v91 op_sel:[0,0,1]
	ds_read_b128 v[80:83], v113 offset:16384
	s_nop 1
	ds_read_b128 v[58:61], v113 offset:16896
	ds_read_b128 v[84:87], v113 offset:17408
	ds_read_b128 v[62:65], v113 offset:17920
	s_mov_b32 s12, 0x43c80000
	v_mfma_f32_16x16x128_f8f6f4 v[200:203], v[124:131], v[72:79], v[200:203]
	v_mfma_f32_32x32x64_f8f6f4 v[4:19], v[104:111], v[132:139], v[4:19]
	v_mfma_f32_32x32x64_f8f6f4 v[20:35], v[140:147], v[132:139], v[20:35]
	s_waitcnt lgkmcnt(6)
	v_mfma_f32_32x32x64_f8f6f4 v[4:19], v[156:163], v[148:155], v[4:19]
	s_waitcnt lgkmcnt(4)
	v_mfma_f32_32x32x64_f8f6f4 v[20:35], v[164:171], v[148:155], v[20:35]
	s_waitcnt lgkmcnt(1)
	v_mfma_f32_32x32x64_f8f6f4 v[4:19], v[80:87], v[72:79], v[4:19]
	s_waitcnt lgkmcnt(0)
	v_mfma_f32_32x32x64_f8f6f4 v[20:35], v[58:65], v[72:79], v[20:35]
	s_nop 1
	v_sub_f32_e32 v37, v200, v204
	v_max3_f32 v0, v0, v52, v37
	v_cmp_nge_f32_e32 vcc, s12, v0
	s_cmp_lg_u64 vcc, 0
	s_cselect_b64 s[12:13], -1, 0
	s_cbranch_vccz .LBB1_12
	s_andn2_b64 vcc, exec, s[12:13]
	s_cbranch_vccnz .LBB1_5

.LBB1_5:
	v_cmp_eq_u32_e32 vcc, 0, v1
	s_nop 1
	s_and_saveexec_b64 s[0:1], vcc
	s_lshl_b32 s12, s29, 2
	s_add_i32 s12, s12, 0x12000
	v_mov_b32_e32 v1, s12
	ds_write_b32 v1, v0
	s_or_b64 exec, exec, s[0:1]
	s_waitcnt vmcnt(0) lgkmcnt(0)
	s_barrier
	v_mov_b32_e32 v104, 0
	v_mov_b32_e32 v206, 0x12000
	ds_read_b128 v[38:41], v206
	ds_read_b128 v[42:45], v206 offset:16
	s_mov_b32 s14, 0
	s_waitcnt lgkmcnt(0)
	v_or_b32_e32 v0, v39, v38
	v_or_b32_e32 v0, v40, v0
	v_or_b32_e32 v0, v41, v0
	v_or_b32_e32 v0, v42, v0
	v_or_b32_e32 v0, v43, v0
	v_or_b32_e32 v0, v44, v0
	v_or_b32_e32 v0, v45, v0
	v_cmp_ne_u32_e32 vcc, 0, v0
	s_cbranch_vccnz .LBB1_13
	s_mov_b64 s[0:1], -1
	v_mov_b64_e32 v[54:55], v[4:5]
	v_mov_b64_e32 v[56:57], v[6:7]
	v_mov_b64_e32 v[58:59], v[8:9]
	v_mov_b64_e32 v[60:61], v[10:11]
	v_mov_b64_e32 v[62:63], v[12:13]
	v_mov_b64_e32 v[64:65], v[14:15]
	v_mov_b64_e32 v[66:67], v[16:17]
	v_mov_b64_e32 v[68:69], v[18:19]
	v_mov_b64_e32 v[38:39], v[20:21]
	v_mov_b64_e32 v[40:41], v[22:23]
	v_mov_b64_e32 v[42:43], v[24:25]
	v_mov_b64_e32 v[44:45], v[26:27]
	v_mov_b64_e32 v[46:47], v[28:29]
	v_mov_b64_e32 v[48:49], v[30:31]
	v_mov_b64_e32 v[50:51], v[32:33]
	v_mov_b64_e32 v[52:53], v[34:35]
	s_branch .Lfinal_copy

.LBB1_12:
	s_cmp_lg_u64 s[0:1], 0
	s_cselect_b64 s[0:1], -1, 0
	v_cndmask_b32_e64 v0, 0, 1, s[0:1]
	s_mov_b32 s0, 0x7f61b1e6
	v_cmp_nge_f32_e32 vcc, s0, v200
	s_cmp_lg_u64 vcc, 0
	s_cselect_b64 s[12:13], -1, 0
	s_andn2_b64 vcc, exec, s[12:13]
	s_cbranch_vccz .LBB1_4
	s_branch .LBB1_5
